# strategy 1: ml_local_unit gate loads issued before the K/V row loads, counted vmcnt(6) instead of vmcnt(0) (on top of v41)
# speedup vs baseline: 1.0070x; 1.0034x over previous
.LBB0_648:
	s_lshr_b32 s2, s5, 30
	s_add_i32 s2, s5, s2
	s_and_b32 s2, s2, -4
	s_sub_i32 s46, s5, s2
	v_readlane_b32 s30, v250, 39
	s_mul_i32 s2, s46, 0x60
	v_readlane_b32 s31, v250, 40
	s_ashr_i32 s3, s2, 31
	v_add_u32_e32 v110, s4, v25
	v_mov_b32_e32 v143, 0
	v_ashrrev_i32_e32 v111, 31, v110
	v_mov_b32_e32 v144, 0
	s_and_saveexec_b64 s[56:57], s[6:7]
	s_cbranch_execz .Lmlg_skip
	v_readlane_b32 s70, v250, 21
	v_lshlrev_b64 v[144:145], 6, v[110:111]
	v_readlane_b32 s71, v250, 22
	v_add_u32_e32 v146, s46, v34
	v_ashrrev_i32_e32 v147, 31, v146
	v_lshl_add_u64 v[144:145], s[70:71], 0, v[144:145]
	v_add_u32_e32 v172, s46, v114
	v_lshl_add_u64 v[146:147], v[146:147], 2, v[144:145]
	v_lshl_add_u64 v[144:145], v[172:173], 2, v[144:145]
	global_load_dword v143, v[146:147], off
	global_load_dword v144, v[144:145], off
.Lmlg_skip:
	s_or_b64 exec, exec, s[56:57]
	v_add_u32_e32 v2, s4, v27
	v_mov_b64_e32 v[0:1], s[30:31]
	v_mad_i64_i32 v[2:3], s[30:31], v2, s66, v[0:1]
	s_lshl_b64 s[2:3], s[2:3], 1
	v_lshl_add_u64 v[2:3], v[2:3], 0, s[2:3]
	v_lshl_add_u64 v[2:3], v[28:29], 1, v[2:3]
	global_load_dwordx4 v[20:23], v[2:3], off offset:768
	global_load_dwordx4 v[16:19], v[2:3], off offset:1536
	v_add_u32_e32 v2, s4, v112
	v_mad_i64_i32 v[2:3], s[30:31], v2, s66, v[0:1]
	v_lshl_add_u64 v[2:3], v[2:3], 0, s[2:3]
	v_lshl_add_u64 v[2:3], v[30:31], 1, v[2:3]
	global_load_dwordx4 v[12:15], v[2:3], off offset:768
	global_load_dwordx4 v[8:11], v[2:3], off offset:1536
	v_add_u32_e32 v2, s4, v113
	v_mad_i64_i32 v[0:1], s[30:31], v2, s66, v[0:1]
	v_lshl_add_u64 v[0:1], v[0:1], 0, s[2:3]
	v_lshl_add_u64 v[0:1], v[32:33], 1, v[0:1]
	global_load_dwordx4 v[4:7], v[0:1], off offset:768
	s_nop 0
	global_load_dwordx4 v[0:3], v[0:1], off offset:1536
	s_and_saveexec_b64 s[4:5], s[6:7]
	s_cbranch_execz .LBB0_656
	s_mov_b32 s0, 0xbfb8aa3b
	s_waitcnt vmcnt(6)
	v_mul_f32_e64 v145, |v144|, s0
	v_exp_f32_e32 v146, v145
	s_mov_b32 s0, 0x3d75c28f
	v_cmp_ngt_f32_e32 vcc, s0, v146
	s_and_saveexec_b64 s[2:3], vcc
	s_xor_b64 s[2:3], exec, s[2:3]
	s_cbranch_execz .LBB0_651
	v_add_f32_e32 v145, 1.0, v146
	s_mov_b32 s0, 0x800000
	v_cmp_gt_f32_e32 vcc, s0, v145
	s_mov_b32 s0, 0x3f317217
	s_nop 0
	v_cndmask_b32_e64 v146, 0, 32, vcc
	v_ldexp_f32 v145, v145, v146
	v_log_f32_e32 v145, v145
	s_nop 0
	v_mul_f32_e32 v146, 0x3f317217, v145
	v_fma_f32 v146, v145, s0, -v146
	v_fmac_f32_e32 v146, 0x3377d1cf, v145
	s_mov_b32 s0, 0x7f800000
	v_fmac_f32_e32 v146, 0x3f317217, v145
	v_cmp_lt_f32_e64 s[30:31], |v145|, s0
	s_nop 1
	v_cndmask_b32_e64 v145, v145, v146, s[30:31]
	v_cndmask_b32_e32 v146, 0, v202, vcc
	v_sub_f32_e32 v145, v145, v146
